# SB attention phase: static s_setprio 1 for waves 4-7 (one wave of each SIMD pair) for the whole phase
# speedup vs baseline: 1.0014x; 1.0014x over previous
; #define LAS __attribute__((address_space(3)))
; __device__ __forceinline__ int launder_v(int v) { asm volatile("" : "+v"(v)); return v; }
; __device__ __forceinline__ void sb_unit(int b, int h, int qb, const bf16_t* __restrict__ PROJ, bf16_t* OCAT, float* SSQO, ldsp shm, volatile LAS unsigned* FL) {
;     const int tid = launder_v(threadIdx.x), lane = tid & 63, r32 = lane & 31, hi = lane >> 5; const int wid = __builtin_amdgcn_readfirstlane(tid >> 6);
;     const size_t rowbase = (size_t)b * SEQ; const int q0 = qb * 256;
;     const bf16_t* ksrc = PROJ + (rowbase + lane) * INP + 1024 + h * 64 + wid * 8;
;     const bf16_t* vsrc = PROJ + (rowbase + 16 * (wid & 3) + (lane >> 2)) * INP + 1536 + h * 64 + (wid >> 2) * 32 + (lane & 3) * 8;
;     const int tmax = 4 * qb + 3, tdw = 4 * qb + (wid >> 1);
;     ...
;     if (tid == 0) { FL[0] = 0u; FL[1] = 0u; FL[2] = 0u; }
.LBB0_1046:
	v_mov_b32_e32 v158, v0
	s_nop 0
	v_readfirstlane_b32 s2, v158
	s_cmpk_lt_u32 s2, 0x100
	s_cbranch_scc1 .Lsb_prio_skip
	s_setprio 1
.Lsb_prio_skip:
	v_cmp_eq_u32_e64 s[36:37], 0, v158
	s_and_saveexec_b64 s[0:1], s[36:37]
	s_cbranch_execz .LBB0_1048
	v_readlane_b32 s4, v255, 2
	s_nop 1
	v_mov_b32_e32 v1, s4
	v_readlane_b32 s4, v255, 3
	ds_write_b32 v1, v3
	s_nop 0
	v_mov_b32_e32 v1, s4
	v_readlane_b32 s4, v255, 4
	ds_write_b32 v1, v3
	s_nop 0
	v_mov_b32_e32 v1, s4
	ds_write_b32 v1, v3

; __device__ __forceinline__ void sb_unit(int b, int h, int qb, const bf16_t* __restrict__ PROJ, bf16_t* OCAT, float* SSQO, ldsp shm, volatile LAS unsigned* FL) {
;     ...
;     asm volatile("s_waitcnt vmcnt(0)" ::: "memory");
;     float sc[16];
; #pragma unroll
;     for (int r = 0; r < 16; ++r) sc[r] = 1.0f;
;     const size_t row0 = rowbase + q0 + wid * 32;
;     store_o(o, sc, OCAT + row0 * 1024 + 512 + h * 64, SSQO + row0 * 16 + 8 + h, shm + SB_OST + wid * 4096, lane, r32, hi);
.LBB0_1073:
	s_setprio 0
	v_readlane_b32 s26, v255, 34
	v_readlane_b32 s27, v255, 35
